# v15_scan
# speedup vs baseline: 1.0323x; 1.0247x over previous
.LBB1_123:
	s_add_i32 s99, s54, s98
	s_lshr_b32 vcc_lo, s99, 2
	s_add_i32 s99, s99, vcc_lo
	s_and_b32 s99, s99, 3
	s_cmp_lg_u32 s99, s86
	s_cbranch_scc1 .LBB1_122
	ds_read2_b32 v[70:71], v68 offset1:4
	ds_read2_b32 v[166:167], v68 offset0:8 offset1:12
	v_add_u32_e32 v72, s97, v67
	v_add_u32_e32 v73, 0x1ed00, v69
	ds_read2_b32 a[0:1], v72 offset1:68
	ds_read2_b32 a[2:3], v72 offset0:136 offset1:204
	ds_read_b32 v73, v73
	v_add_u32_e32 v163, 0x1ed10, v69
	v_add_u32_e32 v164, 0x1ed20, v69
	v_add_u32_e32 v165, 0x1ed30, v69
	ds_read_b32 v163, v163
	ds_read_b32 v164, v164
	ds_read_b32 v165, v165
	s_waitcnt lgkmcnt(0)
	v_xor_b32_e32 v70, 0x80000000, v70
	v_xor_b32_e32 v71, 0x80000000, v71
	v_xor_b32_e32 v166, 0x80000000, v166
	v_xor_b32_e32 v167, 0x80000000, v167
	v_mfma_f32_16x16x4_f32 a[0:3], v70, v73, a[0:3]
	v_mfma_f32_16x16x4_f32 a[0:3], v71, v163, a[0:3]
	v_mfma_f32_16x16x4_f32 a[0:3], v166, v164, a[0:3]
	v_mfma_f32_16x16x4_f32 a[0:3], v167, v165, a[0:3]
	s_nop 9
	ds_write_b32 v72, a0
	ds_write_b32 v72, a1 offset:272
	ds_write_b32 v72, a2 offset:544
	ds_write_b32 v72, a3 offset:816
	s_cmp_eq_u32 s86, 0
	s_cbranch_scc1 .LBB1_97
	s_branch .LBB1_122

.LBB1_244:
	s_add_i32 s99, s52, s98
	s_lshr_b32 vcc_lo, s99, 2
	s_add_i32 s99, s99, vcc_lo
	s_and_b32 s99, s99, 3
	s_cmp_lg_u32 s99, s86
	s_cbranch_scc1 .LBB1_243
	ds_read2_b32 v[6:7], v4 offset1:4
	ds_read2_b32 v[16:17], v4 offset0:8 offset1:12
	v_add_u32_e32 v8, s97, v3
	v_add_u32_e32 v9, 0x1a900, v5
	ds_read2_b32 a[0:1], v8 offset1:68
	ds_read2_b32 a[2:3], v8 offset0:136 offset1:204
	ds_read_b32 v9, v9
	v_add_u32_e32 v13, 0x1a910, v5
	v_add_u32_e32 v14, 0x1a920, v5
	v_add_u32_e32 v15, 0x1a930, v5
	ds_read_b32 v13, v13
	ds_read_b32 v14, v14
	ds_read_b32 v15, v15
	s_waitcnt lgkmcnt(0)
	v_xor_b32_e32 v6, 0x80000000, v6
	v_xor_b32_e32 v7, 0x80000000, v7
	v_xor_b32_e32 v16, 0x80000000, v16
	v_xor_b32_e32 v17, 0x80000000, v17
	v_mfma_f32_16x16x4_f32 a[0:3], v6, v9, a[0:3]
	v_mfma_f32_16x16x4_f32 a[0:3], v7, v13, a[0:3]
	v_mfma_f32_16x16x4_f32 a[0:3], v16, v14, a[0:3]
	v_mfma_f32_16x16x4_f32 a[0:3], v17, v15, a[0:3]
	s_nop 9
	ds_write_b32 v8, a0
	ds_write_b32 v8, a1 offset:272
	ds_write_b32 v8, a2 offset:544
	ds_write_b32 v8, a3 offset:816
	s_cmp_eq_u32 s86, 0
	s_cbranch_scc1 .LBB1_218
	s_branch .LBB1_243

.LBB1_314:
	s_add_i32 s83, s53, s82
	s_lshr_b32 vcc_lo, s83, 2
	s_add_i32 s83, s83, vcc_lo
	s_and_b32 s83, s83, 3
	s_cmp_lg_u32 s83, s86
	s_cbranch_scc1 .LBB1_313
	ds_read2_b32 v[6:7], v4 offset1:4
	ds_read2_b32 v[54:55], v4 offset0:8 offset1:12
	v_add_u32_e32 v8, s81, v3
	v_add_u32_e32 v9, 0x1ed00, v5
	ds_read2_b32 a[0:1], v8 offset1:68
	ds_read2_b32 a[2:3], v8 offset0:136 offset1:204
	ds_read_b32 v9, v9
	v_add_u32_e32 v41, 0x1ed10, v5
	v_add_u32_e32 v42, 0x1ed20, v5
	v_add_u32_e32 v44, 0x1ed30, v5
	ds_read_b32 v41, v41
	ds_read_b32 v42, v42
	ds_read_b32 v44, v44
	s_waitcnt lgkmcnt(0)
	v_xor_b32_e32 v6, 0x80000000, v6
	v_xor_b32_e32 v7, 0x80000000, v7
	v_xor_b32_e32 v54, 0x80000000, v54
	v_xor_b32_e32 v55, 0x80000000, v55
	v_mfma_f32_16x16x4_f32 a[0:3], v6, v9, a[0:3]
	v_mfma_f32_16x16x4_f32 a[0:3], v7, v41, a[0:3]
	v_mfma_f32_16x16x4_f32 a[0:3], v54, v42, a[0:3]
	v_mfma_f32_16x16x4_f32 a[0:3], v55, v44, a[0:3]
	s_nop 9
	ds_write_b32 v8, a0
	ds_write_b32 v8, a1 offset:272
	ds_write_b32 v8, a2 offset:544
	ds_write_b32 v8, a3 offset:816
	s_cmp_eq_u32 s86, 0
	s_cbranch_scc1 .LBB1_288
	s_branch .LBB1_313

.LBB1_355:
	s_add_i32 s81, s53, s80
	s_lshr_b32 vcc_lo, s81, 2
	s_add_i32 s81, s81, vcc_lo
	s_and_b32 s81, s81, 3
	s_cmp_lg_u32 s81, s86
	s_cbranch_scc1 .LBB1_354
	ds_read2_b32 v[4:5], v2 offset1:4
	ds_read2_b32 v[36:37], v2 offset0:8 offset1:12
	v_add_u32_e32 v6, s79, v1
	v_add_u32_e32 v7, 0x1a900, v3
	ds_read2_b32 a[0:1], v6 offset1:68
	ds_read2_b32 a[2:3], v6 offset0:136 offset1:204
	ds_read_b32 v7, v7
	v_add_u32_e32 v14, 0x1a910, v3
	v_add_u32_e32 v34, 0x1a920, v3
	v_add_u32_e32 v35, 0x1a930, v3
	ds_read_b32 v14, v14
	ds_read_b32 v34, v34
	ds_read_b32 v35, v35
	s_waitcnt lgkmcnt(0)
	v_xor_b32_e32 v4, 0x80000000, v4
	v_xor_b32_e32 v5, 0x80000000, v5
	v_xor_b32_e32 v36, 0x80000000, v36
	v_xor_b32_e32 v37, 0x80000000, v37
	v_mfma_f32_16x16x4_f32 a[0:3], v4, v7, a[0:3]
	v_mfma_f32_16x16x4_f32 a[0:3], v5, v14, a[0:3]
	v_mfma_f32_16x16x4_f32 a[0:3], v36, v34, a[0:3]
	v_mfma_f32_16x16x4_f32 a[0:3], v37, v35, a[0:3]
	s_nop 9
	ds_write_b32 v6, a0
	ds_write_b32 v6, a1 offset:272
	ds_write_b32 v6, a2 offset:544
	ds_write_b32 v6, a3 offset:816
	s_cmp_eq_u32 s86, 0
	s_cbranch_scc1 .LBB1_329
	s_branch .LBB1_354
